# speedup vs baseline: 1.0018x; 1.0018x over previous
.LBB0_4:
	s_load_dwordx4 s[8:11], s[0:1], 0x10
	s_load_dwordx2 s[12:13], s[0:1], 0x20
	s_load_dwordx2 s[16:17], s[0:1], 0x8
	s_load_dwordx4 s[20:23], s[0:1], 0x30
	s_load_dwordx2 s[24:25], s[0:1], 0x40
	v_readfirstlane_b32 s26, v0
	s_lshr_b32 s26, s26, 6
	s_and_b32 s27, s4, 0xfffffff3
	s_lshl_b32 s28, s4, 1
	s_and_b32 s28, s28, 8
	s_lshr_b32 s29, s4, 1
	s_and_b32 s29, s29, 4
	s_or_b32 s27, s27, s28
	s_or_b32 s27, s27, s29
	s_lshl_b32 s27, s27, 2
	s_lshr_b32 s30, s4, 4
	s_and_b32 s31, s4, 15
	v_lshlrev_b32_e32 v8, 2, v0
	v_lshlrev_b32_e32 v1, 10, v0
	v_add_u32_e32 v1, s27, v1
	v_and_b32_e32 v2, 0xf3, v0
	v_lshlrev_b32_e32 v3, 1, v0
	v_and_b32_e32 v3, 8, v3
	v_lshrrev_b32_e32 v6, 1, v0
	v_and_b32_e32 v6, 4, v6
	v_or3_b32 v2, v2, v3, v6
	s_lshl_b32 s32, s4, 10
	v_lshl_add_u32 v2, v2, 2, s32
	v_and_b32_e32 v9, 63, v0
	v_lshrrev_b32_e32 v10, 4, v9
	v_and_b32_e32 v11, 15, v9
	v_lshlrev_b32_e32 v10, 10, v10
	v_lshl_or_b32 v13, v11, 2, v10
	v_and_b32_e32 v12, 3, v11
	v_lshlrev_b32_e32 v14, 1, v11
	v_and_b32_e32 v14, 8, v14
	v_lshrrev_b32_e32 v15, 1, v11
	v_and_b32_e32 v15, 4, v15
	v_or3_b32 v12, v12, v14, v15
	v_lshl_or_b32 v12, v12, 2, v10
	v_lshlrev_b32_e32 v3, 2, v9
	s_waitcnt lgkmcnt(0)
	global_load_dword v4, v1, s[10:11]
	global_load_dword v5, v8, s[8:9]
	global_load_dword v7, v2, s[12:13]
	s_lshl_b32 s33, s26, 16
	s_lshl_b32 s34, s30, 6
	s_add_u32 s34, s34, s33
	s_add_u32 s36, s10, s34
	s_addc_u32 s37, s11, 0
	s_lshl_b32 s35, s31, 6
	s_add_u32 s35, s35, s33
	s_add_u32 s38, s16, s35
	s_addc_u32 s39, s17, 0
	global_load_dword v16, v12, s[36:37]
	global_load_dword v32, v13, s[38:39]
	s_add_u32 s36, s36, 0x1000
	s_addc_u32 s37, s37, 0
	s_add_u32 s38, s38, 0x1000
	s_addc_u32 s39, s39, 0
	global_load_dword v17, v12, s[36:37]
	global_load_dword v33, v13, s[38:39]
	s_add_u32 s36, s36, 0x1000
	s_addc_u32 s37, s37, 0
	s_add_u32 s38, s38, 0x1000
	s_addc_u32 s39, s39, 0
	global_load_dword v18, v12, s[36:37]
	global_load_dword v34, v13, s[38:39]
	s_add_u32 s36, s36, 0x1000
	s_addc_u32 s37, s37, 0
	s_add_u32 s38, s38, 0x1000
	s_addc_u32 s39, s39, 0
	global_load_dword v19, v12, s[36:37]
	global_load_dword v35, v13, s[38:39]
	s_add_u32 s36, s36, 0x1000
	s_addc_u32 s37, s37, 0
	s_add_u32 s38, s38, 0x1000
	s_addc_u32 s39, s39, 0
	global_load_dword v20, v12, s[36:37]
	global_load_dword v36, v13, s[38:39]
	s_add_u32 s36, s36, 0x1000
	s_addc_u32 s37, s37, 0
	s_add_u32 s38, s38, 0x1000
	s_addc_u32 s39, s39, 0
	global_load_dword v21, v12, s[36:37]
	global_load_dword v37, v13, s[38:39]
	s_add_u32 s36, s36, 0x1000
	s_addc_u32 s37, s37, 0
	s_add_u32 s38, s38, 0x1000
	s_addc_u32 s39, s39, 0
	global_load_dword v22, v12, s[36:37]
	global_load_dword v38, v13, s[38:39]
	s_add_u32 s36, s36, 0x1000
	s_addc_u32 s37, s37, 0
	s_add_u32 s38, s38, 0x1000
	s_addc_u32 s39, s39, 0
	global_load_dword v23, v12, s[36:37]
	global_load_dword v39, v13, s[38:39]
	s_add_u32 s36, s36, 0x1000
	s_addc_u32 s37, s37, 0
	s_add_u32 s38, s38, 0x1000
	s_addc_u32 s39, s39, 0
	global_load_dword v24, v12, s[36:37]
	global_load_dword v40, v13, s[38:39]
	s_add_u32 s36, s36, 0x1000
	s_addc_u32 s37, s37, 0
	s_add_u32 s38, s38, 0x1000
	s_addc_u32 s39, s39, 0
	global_load_dword v25, v12, s[36:37]
	global_load_dword v41, v13, s[38:39]
	s_add_u32 s36, s36, 0x1000
	s_addc_u32 s37, s37, 0
	s_add_u32 s38, s38, 0x1000
	s_addc_u32 s39, s39, 0
	global_load_dword v26, v12, s[36:37]
	global_load_dword v42, v13, s[38:39]
	s_add_u32 s36, s36, 0x1000
	s_addc_u32 s37, s37, 0
	s_add_u32 s38, s38, 0x1000
	s_addc_u32 s39, s39, 0
	global_load_dword v27, v12, s[36:37]
	global_load_dword v43, v13, s[38:39]
	s_add_u32 s36, s36, 0x1000
	s_addc_u32 s37, s37, 0
	s_add_u32 s38, s38, 0x1000
	s_addc_u32 s39, s39, 0
	global_load_dword v28, v12, s[36:37]
	global_load_dword v44, v13, s[38:39]
	s_add_u32 s36, s36, 0x1000
	s_addc_u32 s37, s37, 0
	s_add_u32 s38, s38, 0x1000
	s_addc_u32 s39, s39, 0
	global_load_dword v29, v12, s[36:37]
	global_load_dword v45, v13, s[38:39]
	s_add_u32 s36, s36, 0x1000
	s_addc_u32 s37, s37, 0
	s_add_u32 s38, s38, 0x1000
	s_addc_u32 s39, s39, 0
	global_load_dword v30, v12, s[36:37]
	global_load_dword v46, v13, s[38:39]
	s_add_u32 s36, s36, 0x1000
	s_addc_u32 s37, s37, 0
	s_add_u32 s38, s38, 0x1000
	s_addc_u32 s39, s39, 0
	global_load_dword v31, v12, s[36:37]
	global_load_dword v47, v13, s[38:39]
	s_waitcnt vmcnt(32)
	v_mul_f32_e32 v6, v4, v5
	v_xor_b32_e32 v14, 0x80, v3
	ds_bpermute_b32 v15, v14, v6
	s_waitcnt vmcnt(30)
	v_mfma_f32_16x16x4_f32 v[48:51], v16, v32, 0
	s_waitcnt vmcnt(28)
	v_mfma_f32_16x16x4_f32 v[48:51], v17, v33, v[48:51]
	s_waitcnt vmcnt(26)
	v_mfma_f32_16x16x4_f32 v[48:51], v18, v34, v[48:51]
	s_waitcnt lgkmcnt(0)
	v_fmac_f32_e32 v15, v4, v5
	v_mov_b32_e32 v6, v15
	v_xor_b32_e32 v14, 0x40, v3
	ds_bpermute_b32 v15, v14, v6
	s_waitcnt vmcnt(24)
	v_mfma_f32_16x16x4_f32 v[48:51], v19, v35, v[48:51]
	s_waitcnt vmcnt(22)
	v_mfma_f32_16x16x4_f32 v[48:51], v20, v36, v[48:51]
	s_waitcnt vmcnt(20)
	v_mfma_f32_16x16x4_f32 v[48:51], v21, v37, v[48:51]
	s_waitcnt lgkmcnt(0)
	v_add_f32_e32 v6, v6, v15
	v_xor_b32_e32 v14, 0x20, v3
	ds_bpermute_b32 v15, v14, v6
	s_waitcnt vmcnt(18)
	v_mfma_f32_16x16x4_f32 v[48:51], v22, v38, v[48:51]
	s_waitcnt vmcnt(16)
	v_mfma_f32_16x16x4_f32 v[48:51], v23, v39, v[48:51]
	s_waitcnt vmcnt(14)
	v_mfma_f32_16x16x4_f32 v[48:51], v24, v40, v[48:51]
	s_waitcnt lgkmcnt(0)
	v_add_f32_e32 v6, v6, v15
	v_xor_b32_e32 v14, 0x10, v3
	ds_bpermute_b32 v15, v14, v6
	s_waitcnt vmcnt(12)
	v_mfma_f32_16x16x4_f32 v[48:51], v25, v41, v[48:51]
	s_waitcnt vmcnt(10)
	v_mfma_f32_16x16x4_f32 v[48:51], v26, v42, v[48:51]
	s_waitcnt vmcnt(8)
	v_mfma_f32_16x16x4_f32 v[48:51], v27, v43, v[48:51]
	s_waitcnt lgkmcnt(0)
	v_add_f32_e32 v6, v6, v15
	v_xor_b32_e32 v14, 0x8, v3
	ds_bpermute_b32 v15, v14, v6
	s_waitcnt vmcnt(6)
	v_mfma_f32_16x16x4_f32 v[48:51], v28, v44, v[48:51]
	s_waitcnt vmcnt(4)
	v_mfma_f32_16x16x4_f32 v[48:51], v29, v45, v[48:51]
	s_waitcnt vmcnt(2)
	v_mfma_f32_16x16x4_f32 v[48:51], v30, v46, v[48:51]
	s_waitcnt lgkmcnt(0)
	v_add_f32_e32 v6, v6, v15
	v_xor_b32_e32 v14, 0x4, v3
	ds_bpermute_b32 v15, v14, v6
	s_waitcnt vmcnt(0)
	v_mfma_f32_16x16x4_f32 v[48:51], v31, v47, v[48:51]
	s_waitcnt lgkmcnt(0)
	v_add_f32_e32 v6, v6, v15
	s_lshl_b32 s33, s26, 2
	v_mov_b32_e32 v14, s33
	ds_write_b32 v14, v6 offset:21504
	s_lshl_b32 s33, s26, 10
	v_lshrrev_b32_e32 v14, 4, v9
	v_lshlrev_b32_e32 v14, 8, v14
	v_lshl_or_b32 v14, v11, 2, v14
	v_add_u32_e32 v14, s33, v14
	s_nop 10
	ds_write_b32 v14, v48 offset:16384
	ds_write_b32 v14, v49 offset:16448
	ds_write_b32 v14, v50 offset:16512
	ds_write_b32 v14, v51 offset:16576
	s_waitcnt lgkmcnt(0)
	s_barrier
	ds_read2st64_b32 v[16:17], v8 offset0:64 offset1:68
	ds_read2st64_b32 v[18:19], v8 offset0:72 offset1:76
	v_mov_b32_e32 v20, 0
	ds_read_b128 v[24:27], v20 offset:21504
	v_lshlrev_b32_e32 v1, 1, v0
	s_lshl_b32 s33, s4, 9
	v_add_u32_e32 v1, s33, v1
	v_cvt_pk_bf16_f32 v7, v7, v7
	global_store_short v1, v7, s[24:25]
	v_lshrrev_b32_e32 v2, 4, v0
	v_lshlrev_b32_e32 v2, 9, v2
	v_and_b32_e32 v21, 15, v0
	v_lshl_or_b32 v2, v21, 1, v2
	s_lshl_b32 s33, s30, 13
	s_lshl_b32 s34, s31, 5
	s_add_u32 s33, s33, s34
	v_add_u32_e32 v2, s33, v2
	s_waitcnt lgkmcnt(2)
	v_add_f32_e32 v16, v16, v17
	s_waitcnt lgkmcnt(1)
	v_add_f32_e32 v16, v16, v18
	v_add_f32_e32 v16, v16, v19
	v_mul_f32_e32 v16, 0x3db8aa3b, v16
	v_cvt_pk_bf16_f32 v16, v16, v16
	global_store_short v2, v16, s[20:21]
	s_waitcnt lgkmcnt(0)
	v_add_f32_e32 v24, v24, v25
	v_add_f32_e32 v24, v24, v26
	v_add_f32_e32 v24, v24, v27
	v_mul_f32_e32 v24, 0x3db8aa3b, v24
	s_lshl_b32 s33, s4, 2
	v_mov_b32_e32 v25, s33
	v_cmp_eq_u32_e32 vcc, 0, v0
	s_and_saveexec_b64 s[40:41], vcc
	global_store_dword v25, v24, s[22:23]
	s_endpgm
